# P5 scan output stores: 32-bit offset + SGPR base (saddr form) instead of per-store 64-bit address math (-2 VALU incl. both 64-bit ops per store, 32 stores per step on the serial chain); on top of v123
# speedup vs baseline: 1.0076x; 1.0076x over previous
; __device__ __forceinline__ bf16_t f2bf(float a) { return (bf16_t)(pk(a, 0.f) & 0xffffu); }
; __device__ __forceinline__ void p4_scan(Frame& F) {
;     ...
;     const int nt = F.wave, c = lane & 31, hh = lane >> 5;
;     bf16_t* OGb = WSP(bf16_t, WS_OGB) + (size_t)dir * ML * 1024;
;     f32x16 S[4];
; #pragma unroll
;     for (int kt = 0; kt < 4; ++kt)
; #pragma unroll
;         for (int i = 0; i < 16; ++i) S[kt][i] = 0.f;
;     bool stored = false;
;     ...
;         if (cidx >= CTXL / 64) { const int rowbase = b * SEQ + (cidx - CTXL / 64) * 64;
; #pragma unroll
;             for (int mt = 0; mt < 2; ++mt)
; #pragma unroll
;                 for (int reg = 0; reg < 16; ++reg) { const int row = 32 * mt + (reg & 3) + 8 * (reg >> 2) + 4 * hh, prow = rowbase + (dir ? 63 - row : row);
;                     OGb[(size_t)prow * 1024 + h * 128 + 32 * nt + c] = f2bf(O[mt][reg]); } }
.LBB0_628:
	v_readlane_b32 s34, v253, 0
	s_mov_b64 s[28:29], -1
	s_cmpk_lt_u32 s34, 0x100
	v_lshl_add_u64 v[138:139], s[26:27], 0, v[140:141]
	s_cbranch_scc0 .LBB0_644
	s_lshl_b32 s26, s58, 25
	s_add_u32 s26, s86, s26
	s_addc_u32 s28, s87, 0
	v_readlane_b32 s34, v253, 7
	s_lshl_b32 s61, s31, 13
	s_and_b32 s59, s80, 15
	s_lshl_b32 s60, s34, 11
	s_addk_i32 s61, 0xff00
	s_lshl_b32 s29, s30, 8
	s_add_u32 s26, s26, s29
	s_addc_u32 s29, s28, 0
	s_lshl_b32 s28, s34, 6
	v_and_b32_e32 v2, 31, v0
	s_add_u32 s28, s26, s28
	v_lshrrev_b32_e32 v6, 3, v162
	s_addc_u32 s29, s29, 0
	v_lshlrev_b32_e32 v2, 1, v2
	v_mov_b32_e32 v3, 0
	v_and_b32_e32 v7, 4, v6
	v_lshl_add_u64 v[4:5], s[28:29], 0, v[2:3]
	v_mov_b32_e32 v142, v2
	s_add_u32 s98, s28, 0x59000000
	s_addc_u32 s99, s29, 0
	s_mov_b64 s[28:29], 0x59000000
	v_bitop3_b32 v2, v6, 63, 4 bitop3:0x6c
	v_cndmask_b32_e64 v141, v2, v7, s[0:1]
	v_or_b32_e32 v2, 1, v7
	v_bitop3_b32 v4, v6, 62, 4 bitop3:0x6c
	v_cndmask_b32_e64 v144, v4, v2, s[0:1]
	v_or_b32_e32 v2, 2, v7
	v_bitop3_b32 v4, v6, 61, 4 bitop3:0x6c
	v_cndmask_b32_e64 v145, v4, v2, s[0:1]
	v_or_b32_e32 v2, 3, v6
	v_bitop3_b32 v4, v6, 63, 3 bitop3:0x36
	v_cndmask_b32_e64 v146, v4, v2, s[0:1]
	v_or_b32_e32 v2, 8, v7
	v_bitop3_b32 v4, v6, 55, 4 bitop3:0x6c
	v_cndmask_b32_e64 v147, v4, v2, s[0:1]
	v_or_b32_e32 v2, 9, v7
	v_bitop3_b32 v4, v6, 54, 4 bitop3:0x6c
	v_cndmask_b32_e64 v148, v4, v2, s[0:1]
	v_or_b32_e32 v2, 10, v7
	v_bitop3_b32 v4, v6, 53, 4 bitop3:0x6c
	v_cndmask_b32_e64 v149, v4, v2, s[0:1]
	v_or_b32_e32 v2, 11, v6
	v_bitop3_b32 v4, v6, 55, 3 bitop3:0x36
	v_cndmask_b32_e64 v150, v4, v2, s[0:1]
	v_or_b32_e32 v2, 16, v7
	v_bitop3_b32 v4, v6, 47, 4 bitop3:0x6c
	v_cndmask_b32_e64 v151, v4, v2, s[0:1]
	v_or_b32_e32 v2, 17, v7
	v_bitop3_b32 v4, v6, 46, 4 bitop3:0x6c
	v_cndmask_b32_e64 v152, v4, v2, s[0:1]
	v_or_b32_e32 v2, 18, v7
	v_bitop3_b32 v4, v6, 45, 4 bitop3:0x6c
	v_cndmask_b32_e64 v153, v4, v2, s[0:1]
	v_or_b32_e32 v2, 19, v6
	v_bitop3_b32 v4, v6, 47, 3 bitop3:0x36
	v_cndmask_b32_e64 v154, v4, v2, s[0:1]
	v_or_b32_e32 v2, 24, v7
	v_bitop3_b32 v4, v6, 39, 4 bitop3:0x6c
	v_cndmask_b32_e64 v155, v4, v2, s[0:1]
	v_or_b32_e32 v2, 25, v7
	v_bitop3_b32 v4, v6, 38, 4 bitop3:0x6c
	v_cndmask_b32_e64 v156, v4, v2, s[0:1]
	v_or_b32_e32 v2, 26, v7
	v_bitop3_b32 v4, v6, 37, 4 bitop3:0x6c
	v_cndmask_b32_e64 v157, v4, v2, s[0:1]
	v_or_b32_e32 v2, 27, v6
	v_bitop3_b32 v4, v6, 39, 3 bitop3:0x36
	v_cndmask_b32_e64 v158, v4, v2, s[0:1]
	v_or_b32_e32 v2, 32, v7
	v_bitop3_b32 v4, v6, 31, 4 bitop3:0x6c
	v_cndmask_b32_e64 v159, v4, v2, s[0:1]
	v_or_b32_e32 v2, 33, v7
	v_bitop3_b32 v4, v6, 30, 4 bitop3:0x6c
	v_cndmask_b32_e64 v160, v4, v2, s[0:1]
	v_or_b32_e32 v2, 34, v7
	v_bitop3_b32 v4, v6, 29, 4 bitop3:0x6c
	v_cndmask_b32_e64 v161, v4, v2, s[0:1]
	v_or_b32_e32 v2, 35, v6
	v_bitop3_b32 v4, v6, 63, 35 bitop3:0x36
	v_cndmask_b32_e64 v163, v4, v2, s[0:1]
	v_or_b32_e32 v2, 40, v7
	v_bitop3_b32 v4, v6, 23, 4 bitop3:0x6c
	v_cndmask_b32_e64 v164, v4, v2, s[0:1]
	v_or_b32_e32 v2, 41, v7
	v_bitop3_b32 v4, v6, 22, 4 bitop3:0x6c
	v_cndmask_b32_e64 v165, v4, v2, s[0:1]
	v_or_b32_e32 v2, 42, v7
	v_bitop3_b32 v4, v6, 21, 4 bitop3:0x6c
	v_cndmask_b32_e64 v166, v4, v2, s[0:1]
	v_or_b32_e32 v2, 43, v6
	v_bitop3_b32 v4, v6, 20, 4 bitop3:0x6c
	v_cndmask_b32_e64 v167, v4, v2, s[0:1]
	v_or_b32_e32 v2, 48, v7
	v_bitop3_b32 v4, v6, 15, 4 bitop3:0x6c
	v_cndmask_b32_e64 v168, v4, v2, s[0:1]
	v_or_b32_e32 v2, 49, v7
	v_bitop3_b32 v4, v6, 14, 4 bitop3:0x6c
	v_cndmask_b32_e64 v169, v4, v2, s[0:1]
	v_or_b32_e32 v2, 50, v7
	v_bitop3_b32 v4, v6, 13, 4 bitop3:0x6c
	v_cndmask_b32_e64 v170, v4, v2, s[0:1]
	v_or_b32_e32 v2, 51, v6
	v_bitop3_b32 v4, v6, 12, 4 bitop3:0x6c
	v_cndmask_b32_e64 v171, v4, v2, s[0:1]
	v_or_b32_e32 v2, 56, v7
	v_bitop3_b32 v4, v6, 7, 4 bitop3:0x6c
	v_cndmask_b32_e64 v172, v4, v2, s[0:1]
	v_or_b32_e32 v2, 57, v7
	v_bitop3_b32 v4, v6, 6, 4 bitop3:0x6c
	v_cndmask_b32_e64 v173, v4, v2, s[0:1]
	v_or_b32_e32 v2, 58, v7
	v_bitop3_b32 v4, v6, 5, 4 bitop3:0x6c
	s_mov_b32 s27, 0
	s_lshl_b32 s26, s34, 10
	v_cndmask_b32_e64 v174, v4, v2, s[0:1]
	v_or_b32_e32 v2, 59, v6
	v_bitop3_b32 v4, v6, 4, v6 bitop3:0xc
	v_lshlrev_b32_e32 v1, 5, v162
	s_lshl_b32 s28, s50, 10
	s_mov_b32 s29, s27
	s_lshl_b32 s30, s51, 10
	s_mov_b32 s31, s27
	s_lshl_b32 s34, s52, 10
	s_mov_b32 s35, s27
	s_lshl_b32 s36, s53, 10
	s_mov_b32 s37, s27
	s_lshl_b32 s38, s54, 10
	s_mov_b32 s39, s27
	s_lshl_b32 s40, s55, 10
	s_mov_b32 s41, s27
	s_lshl_b32 s42, s56, 10
	s_mov_b32 s43, s27
	s_lshl_b32 s44, s57, 10
	s_mov_b32 s45, s27
	s_or_b32 s46, s26, 0x12000
	s_mov_b32 s47, s27
	v_cndmask_b32_e64 v175, v4, v2, s[0:1]
	s_mov_b64 s[48:49], 0
	s_movk_i32 s62, 0x86
	v_mov_b32_e32 v176, 0x12400
	s_mov_b32 s64, s27
	v_mov_b32_e32 v2, v3
	v_mov_b32_e32 v4, v3
	v_mov_b32_e32 v5, v3
	v_mov_b32_e32 v6, v3
	v_mov_b32_e32 v7, v3
	v_mov_b32_e32 v8, v3
	v_mov_b32_e32 v9, v3
	v_mov_b32_e32 v10, v3
	v_mov_b32_e32 v11, v3
	v_mov_b32_e32 v12, v3
	v_mov_b32_e32 v13, v3
	v_mov_b32_e32 v14, v3
	v_mov_b32_e32 v15, v3
	v_mov_b32_e32 v16, v3
	v_mov_b32_e32 v17, v3
	v_mov_b32_e32 v18, v3
	v_mov_b32_e32 v19, v3
	v_mov_b32_e32 v20, v3
	v_mov_b32_e32 v21, v3
	v_mov_b32_e32 v22, v3
	v_mov_b32_e32 v23, v3
	v_mov_b32_e32 v24, v3
	v_mov_b32_e32 v25, v3
	v_mov_b32_e32 v26, v3
	v_mov_b32_e32 v27, v3
	v_mov_b32_e32 v28, v3
	v_mov_b32_e32 v29, v3
	v_mov_b32_e32 v30, v3
	v_mov_b32_e32 v31, v3
	v_mov_b32_e32 v32, v3
	v_mov_b32_e32 v33, v3
	v_mov_b32_e32 v34, v3
	v_mov_b32_e32 v35, v3
	v_mov_b32_e32 v36, v3
	v_mov_b32_e32 v37, v3
	v_mov_b32_e32 v38, v3
	v_mov_b32_e32 v39, v3
	v_mov_b32_e32 v40, v3
	v_mov_b32_e32 v41, v3
	v_mov_b32_e32 v42, v3
	v_mov_b32_e32 v43, v3
	v_mov_b32_e32 v44, v3
	v_mov_b32_e32 v45, v3
	v_mov_b32_e32 v46, v3
	v_mov_b32_e32 v47, v3
	v_mov_b32_e32 v48, v3
	v_mov_b32_e32 v49, v3
	v_mov_b32_e32 v50, v3
	v_mov_b32_e32 v51, v3
	v_mov_b32_e32 v52, v3
	v_mov_b32_e32 v53, v3
	v_mov_b32_e32 v54, v3
	v_mov_b32_e32 v55, v3
	v_mov_b32_e32 v56, v3
	v_mov_b32_e32 v57, v3
	v_mov_b32_e32 v58, v3
	v_mov_b32_e32 v59, v3
	v_mov_b32_e32 v60, v3
	v_mov_b32_e32 v61, v3
	v_mov_b32_e32 v62, v3
	v_mov_b32_e32 v63, v3
	v_mov_b32_e32 v64, v3
	v_mov_b32_e32 v65, v3
	s_branch .LBB0_631

; #define LAS __attribute__((address_space(3)))
; __device__ __forceinline__ float bf_lo(unsigned w) { return __uint_as_float(w << 16); }
; __device__ __forceinline__ float bf_hi(unsigned w) { return __uint_as_float(w & 0xffff0000u); }
; #define MFMA32(a, b, c) __builtin_amdgcn_mfma_f32_32x32x16_bf16((a), (b), (c), 0, 0, 0)
; __device__ __forceinline__ bf16x8 pack_step(const f32x16& x, int s) { return __builtin_bit_cast(bf16x8, ((u32x4){pk(x[8 * s], x[8 * s + 1]), pk(x[8 * s + 2], x[8 * s + 3]), pk(x[8 * s + 4], x[8 * s + 5]), pk(x[8 * s + 6], x[8 * s + 7])})); }
; __device__ __forceinline__ void p4_scan(Frame& F) {
;     ...
;         const LAS unsigned char* lb = F.lds + (n & 1) * UNIT_DMA;
;         const float dlc = *(const LAS float*)(lb + UO_DL);
;         u32x4 ucur[2][2];
; #pragma unroll
;         for (int mt = 0; mt < 2; ++mt) { ucur[mt][0] = *(const LAS u32x4*)(lb + UO_U + (mt * 4 + nt) * 2048 + lane * 32); ucur[mt][1] = *(const LAS u32x4*)(lb + UO_U + (mt * 4 + nt) * 2048 + lane * 32 + 16); }
;     ...
;         f32x16 VN[2], O[2];
; #pragma unroll
;         for (int mt = 0; mt < 2; ++mt) {
; #pragma unroll
;             for (int p = 0; p < 4; ++p) { VN[mt][2 * p] = bf_lo(ucur[mt][0][p]); VN[mt][2 * p + 1] = bf_hi(ucur[mt][0][p]); VN[mt][8 + 2 * p] = bf_lo(ucur[mt][1][p]); VN[mt][8 + 2 * p + 1] = bf_hi(ucur[mt][1][p]); }
; #pragma unroll
;             for (int i = 0; i < 16; ++i) O[mt][i] = 0.f; }
; #pragma unroll
;         for (int kt = 0; kt < 4; ++kt) { const bf16x8 sb0 = pack_step(S[kt], 0), sb1 = pack_step(S[kt], 1);
; #pragma unroll
;             for (int mt = 0; mt < 2; ++mt) { const int fi = (mt * 4 + kt) * 2;
;                 VN[mt] = MFMA32(FRAG(UO_NW, fi), sb0, VN[mt]); VN[mt] = MFMA32(FRAG(UO_NW, fi + 1), sb1, VN[mt]);
;                 O[mt] = MFMA32(FRAG(UO_QD, fi), sb0, O[mt]); O[mt] = MFMA32(FRAG(UO_QD, fi + 1), sb1, O[mt]); } }
.LBB0_641:
	s_bitcmp1_b32 s64, 0
	s_cselect_b32 s48, 0x12400, 0
	s_add_i32 s48, s48, 0
	s_add_i32 s49, s48, s60
	v_add_u32_e32 v66, s49, v1
	v_add_u32_e32 v177, s48, v140
	ds_read_b128 v[70:73], v66 offset:57344
	v_add_u32_e32 v67, 0xe000, v66
	ds_read_b128 v[78:81], v66 offset:57360
	ds_read_b128 v[86:89], v67 offset:8192
	ds_read_b128 v[82:85], v67 offset:8208
	ds_read_b128 v[94:97], v177
	v_cvt_pk_bf16_f32 v90, v2, v3
	s_waitcnt lgkmcnt(0)
	v_lshlrev_b32_e32 v66, 16, v70
	v_and_b32_e32 v67, 0xffff0000, v70
	v_lshlrev_b32_e32 v74, 16, v78
	v_and_b32_e32 v75, 0xffff0000, v78
	v_lshlrev_b32_e32 v68, 16, v71
	v_and_b32_e32 v69, 0xffff0000, v71
	v_lshlrev_b32_e32 v76, 16, v79
	v_and_b32_e32 v77, 0xffff0000, v79
	v_lshlrev_b32_e32 v70, 16, v72
	v_and_b32_e32 v71, 0xffff0000, v72
	v_lshlrev_b32_e32 v78, 16, v80
	v_and_b32_e32 v79, 0xffff0000, v80
	v_lshlrev_b32_e32 v72, 16, v73
	v_and_b32_e32 v73, 0xffff0000, v73
	v_lshlrev_b32_e32 v80, 16, v81
	v_and_b32_e32 v81, 0xffff0000, v81
	v_cvt_pk_bf16_f32 v91, v4, v5
	v_cvt_pk_bf16_f32 v92, v6, v7
	v_cvt_pk_bf16_f32 v93, v8, v9
	ds_read_b128 v[98:101], v177 offset:1024
	ds_read_b128 v[130:133], v177 offset:56320
	v_mfma_f32_32x32x16_bf16 v[66:81], v[94:97], v[90:93], v[66:81]
	ds_read_b128 v[94:97], v177 offset:16384
	ds_read_b128 v[182:185], v177 offset:2048
	v_cvt_pk_bf16_f32 v178, v10, v11
	v_cvt_pk_bf16_f32 v179, v12, v13
	v_cvt_pk_bf16_f32 v180, v14, v15
	v_cvt_pk_bf16_f32 v181, v16, v17
	ds_read_b128 v[134:137], v177 offset:32768
	ds_read_b128 v[126:129], v177 offset:17408
	ds_read_b128 v[186:189], v177 offset:15360
	s_waitcnt lgkmcnt(0)
	v_mfma_f32_32x32x16_bf16 v[66:81], v[98:101], v[178:181], v[66:81]
	v_lshlrev_b32_e32 v114, 16, v86
	v_and_b32_e32 v115, 0xffff0000, v86
	v_lshlrev_b32_e32 v122, 16, v82
	v_and_b32_e32 v123, 0xffff0000, v82
	v_lshlrev_b32_e32 v116, 16, v87
	v_and_b32_e32 v117, 0xffff0000, v87
	v_lshlrev_b32_e32 v124, 16, v83
	v_mfma_f32_32x32x16_bf16 v[98:113], v[94:97], v[90:93], 0
	ds_read_b128 v[94:97], v177 offset:8192
	ds_read_b128 v[190:193], v177 offset:18432
	v_and_b32_e32 v125, 0xffff0000, v83
	v_lshlrev_b32_e32 v118, 16, v88
	v_and_b32_e32 v119, 0xffff0000, v88
	v_lshlrev_b32_e32 v120, 16, v89
	v_and_b32_e32 v121, 0xffff0000, v89
	ds_read_b128 v[194:197], v177 offset:7168
	v_mfma_f32_32x32x16_bf16 v[98:113], v[126:129], v[178:181], v[98:113]
	v_lshlrev_b32_e32 v126, 16, v84
	v_and_b32_e32 v127, 0xffff0000, v84
	v_lshlrev_b32_e32 v128, 16, v85
	v_and_b32_e32 v129, 0xffff0000, v85
	ds_read_b128 v[82:85], v177 offset:9216
	ds_read_b128 v[198:201], v177 offset:10240
	s_add_i32 s48, s48, 0x12000
	s_cmp_gt_u32 s64, 3
	s_waitcnt lgkmcnt(0)
	v_mfma_f32_32x32x16_bf16 v[114:129], v[94:97], v[90:93], v[114:129]
	v_mfma_f32_32x32x16_bf16 v[114:129], v[82:85], v[178:181], v[114:129]
	ds_read_b128 v[82:85], v177 offset:24576
	ds_read_b128 v[202:205], v177 offset:23552
	ds_read_b128 v[206:209], v177 offset:25600
	ds_read_b128 v[210:213], v177 offset:26624
	ds_read_b128 v[214:217], v177 offset:4096
	s_waitcnt lgkmcnt(0)
	v_mfma_f32_32x32x16_bf16 v[82:97], v[82:85], v[90:93], 0
	v_mfma_f32_32x32x16_bf16 v[82:97], v[206:209], v[178:181], v[82:97]
	v_cvt_pk_bf16_f32 v178, v18, v19
	v_cvt_pk_bf16_f32 v179, v20, v21
	v_cvt_pk_bf16_f32 v180, v22, v23
	v_cvt_pk_bf16_f32 v181, v24, v25
	v_cvt_pk_bf16_f32 v206, v26, v27
	v_cvt_pk_bf16_f32 v207, v28, v29
	v_cvt_pk_bf16_f32 v208, v30, v31
	v_mfma_f32_32x32x16_bf16 v[66:81], v[182:185], v[178:181], v[66:81]
	ds_read_b128 v[182:185], v177 offset:3072
	v_cvt_pk_bf16_f32 v209, v32, v33
	v_mfma_f32_32x32x16_bf16 v[98:113], v[190:193], v[178:181], v[98:113]
	s_waitcnt lgkmcnt(0)
	v_mfma_f32_32x32x16_bf16 v[66:81], v[182:185], v[206:209], v[66:81]
	ds_read_b128 v[182:185], v177 offset:19456
	ds_read_b128 v[190:193], v177 offset:20480
	v_mfma_f32_32x32x16_bf16 v[114:129], v[198:201], v[178:181], v[114:129]
	s_waitcnt lgkmcnt(0)
	v_mfma_f32_32x32x16_bf16 v[98:113], v[182:185], v[206:209], v[98:113]
	ds_read_b128 v[182:185], v177 offset:11264
	ds_read_b128 v[198:201], v177 offset:12288
	v_mfma_f32_32x32x16_bf16 v[82:97], v[210:213], v[178:181], v[82:97]
	v_cvt_pk_bf16_f32 v210, v42, v43
	v_cvt_pk_bf16_f32 v211, v44, v45
	v_cvt_pk_bf16_f32 v212, v46, v47
	v_cvt_pk_bf16_f32 v213, v48, v49
	s_waitcnt lgkmcnt(0)
	v_mfma_f32_32x32x16_bf16 v[114:129], v[182:185], v[206:209], v[114:129]
	ds_read_b128 v[178:181], v177 offset:27648
	ds_read_b128 v[182:185], v177 offset:28672
	s_waitcnt lgkmcnt(0)
	v_mfma_f32_32x32x16_bf16 v[82:97], v[178:181], v[206:209], v[82:97]
	v_cvt_pk_bf16_f32 v178, v34, v35
	v_cvt_pk_bf16_f32 v179, v36, v37
	v_cvt_pk_bf16_f32 v180, v38, v39
	v_cvt_pk_bf16_f32 v181, v40, v41
	ds_read_b128 v[206:209], v177 offset:5120
	s_nop 0
	v_mfma_f32_32x32x16_bf16 v[66:81], v[214:217], v[178:181], v[66:81]
	ds_read_b128 v[214:217], v177 offset:6144
	v_mfma_f32_32x32x16_bf16 v[98:113], v[190:193], v[178:181], v[98:113]
	s_waitcnt lgkmcnt(0)
	v_mfma_f32_32x32x16_bf16 v[66:81], v[206:209], v[210:213], v[66:81]
	ds_read_b128 v[190:193], v177 offset:21504
	ds_read_b128 v[206:209], v177 offset:22528
	v_mfma_f32_32x32x16_bf16 v[114:129], v[198:201], v[178:181], v[114:129]
	v_mfma_f32_32x32x16_bf16 v[82:97], v[182:185], v[178:181], v[82:97]
	s_waitcnt lgkmcnt(0)
	v_mfma_f32_32x32x16_bf16 v[98:113], v[190:193], v[210:213], v[98:113]
	ds_read_b128 v[190:193], v177 offset:13312
	ds_read_b128 v[198:201], v177 offset:14336
	ds_read_b128 v[178:181], v177 offset:29696
	ds_read_b128 v[182:185], v177 offset:30720
	s_waitcnt lgkmcnt(0)
; #define MFMA32(a, b, c) __builtin_amdgcn_mfma_f32_32x32x16_bf16((a), (b), (c), 0, 0, 0)
; __device__ __forceinline__ bf16x8 pack_step(const f32x16& x, int s) { return __builtin_bit_cast(bf16x8, ((u32x4){pk(x[8 * s], x[8 * s + 1]), pk(x[8 * s + 2], x[8 * s + 3]), pk(x[8 * s + 4], x[8 * s + 5]), pk(x[8 * s + 6], x[8 * s + 7])})); }
; __device__ __forceinline__ void p4_scan(Frame& F) {
;     ...
;         bf16x8 vb[2][2];
; #pragma unroll
;         for (int ct = 0; ct < 2; ++ct) { vb[ct][0] = pack_step(VN[ct], 0); vb[ct][1] = pack_step(VN[ct], 1); }
; #pragma unroll
;         for (int mt = 0; mt < 2; ++mt)
; #pragma unroll
;             for (int ct = 0; ct < 2; ++ct) { const int fi = (mt * 2 + ct) * 2; O[mt] = MFMA32(FRAG(UO_QK, fi), vb[ct][0], O[mt]); O[mt] = MFMA32(FRAG(UO_QK, fi + 1), vb[ct][1], O[mt]); }
; #pragma unroll
;         for (int kt = 0; kt < 4; ++kt) {
; #pragma unroll
;             for (int i = 0; i < 16; ++i) S[kt][i] *= dlc;
; #pragma unroll
;             for (int ct = 0; ct < 2; ++ct) { const int fi = (kt * 2 + ct) * 2; S[kt] = MFMA32(FRAG(UO_KDT, fi), vb[ct][0], S[kt]); S[kt] = MFMA32(FRAG(UO_KDT, fi + 1), vb[ct][1], S[kt]); } }
;     ...
;         const int cidx = STEP_CIDX(n);
;         stored = cidx >= CTXL / 64;
	v_mfma_f32_32x32x16_bf16 v[114:129], v[190:193], v[210:213], v[114:129]
	v_cvt_pk_bf16_f32 v190, v58, v59
	v_cvt_pk_bf16_f32 v191, v60, v61
	v_cvt_pk_bf16_f32 v192, v62, v63
	v_cvt_pk_bf16_f32 v193, v64, v65
	v_mfma_f32_32x32x16_bf16 v[82:97], v[178:181], v[210:213], v[82:97]
	v_cvt_pk_bf16_f32 v178, v50, v51
	v_cvt_pk_bf16_f32 v179, v52, v53
	v_cvt_pk_bf16_f32 v180, v54, v55
	v_cvt_pk_bf16_f32 v181, v56, v57
	s_nop 1
	v_mfma_f32_32x32x16_bf16 v[66:81], v[214:217], v[178:181], v[66:81]
	v_mfma_f32_32x32x16_bf16 v[98:113], v[206:209], v[178:181], v[98:113]
	v_mfma_f32_32x32x16_bf16 v[114:129], v[198:201], v[178:181], v[114:129]
	v_mfma_f32_32x32x16_bf16 v[82:97], v[182:185], v[178:181], v[82:97]
	ds_read_b128 v[178:181], v177 offset:31744
	v_mfma_f32_32x32x16_bf16 v[66:81], v[194:197], v[190:193], v[66:81]
	s_waitcnt lgkmcnt(0)
	v_mfma_f32_32x32x16_bf16 v[82:97], v[178:181], v[190:193], v[82:97]
	ds_read_b128 v[178:181], v177 offset:49152
	s_nop 8
	v_cvt_pk_bf16_f32 v66, v66, v67
	v_cvt_pk_bf16_f32 v67, v68, v69
	v_cvt_pk_bf16_f32 v68, v70, v71
	v_cvt_pk_bf16_f32 v69, v72, v73
	ds_read_b128 v[70:73], v177 offset:48128
	v_cvt_pk_bf16_f32 v74, v74, v75
	v_mfma_f32_32x32x16_bf16 v[98:113], v[202:205], v[190:193], v[98:113]
	v_cvt_pk_bf16_f32 v75, v76, v77
	v_cvt_pk_bf16_f32 v76, v78, v79
	v_cvt_pk_bf16_f32 v77, v80, v81
	ds_read_b128 v[78:81], v177 offset:51200
	s_waitcnt lgkmcnt(0)
	v_mfma_f32_32x32x16_bf16 v[98:113], v[178:181], v[66:69], v[98:113]
	ds_read_b128 v[178:181], v177 offset:50176
	v_mfma_f32_32x32x16_bf16 v[114:129], v[186:189], v[190:193], v[114:129]
	s_waitcnt lgkmcnt(0)
	v_mfma_f32_32x32x16_bf16 v[98:113], v[178:181], v[74:77], v[98:113]
	s_nop 9
	v_cvt_pk_bf16_f32 v114, v114, v115
	v_cvt_pk_bf16_f32 v115, v116, v117
	v_cvt_pk_bf16_f32 v116, v118, v119
	v_cvt_pk_bf16_f32 v117, v120, v121
	v_cvt_pk_bf16_f32 v118, v122, v123
	v_cvt_pk_bf16_f32 v119, v124, v125
	ds_read_b128 v[122:125], v177 offset:53248
	v_mfma_f32_32x32x16_bf16 v[98:113], v[78:81], v[114:117], v[98:113]
	ds_read_b128 v[78:81], v177 offset:52224
	v_cvt_pk_bf16_f32 v120, v126, v127
	v_cvt_pk_bf16_f32 v121, v128, v129
	s_waitcnt lgkmcnt(0)
	v_mfma_f32_32x32x16_bf16 v[82:97], v[122:125], v[66:69], v[82:97]
	v_mfma_f32_32x32x16_bf16 v[98:113], v[78:81], v[118:121], v[98:113]
	ds_read_b128 v[78:81], v177 offset:54272
	ds_read_b128 v[122:125], v177 offset:55296
	s_waitcnt lgkmcnt(0)
	v_mfma_f32_32x32x16_bf16 v[82:97], v[78:81], v[74:77], v[82:97]
	v_mov_b32_e32 v78, s48
	ds_read_b32 v126, v78
	s_cselect_b32 s48, 0x87, 3
	s_add_i32 s48, s48, s62
	s_add_i32 s65, s48, 0xffffff7a
	s_and_b64 s[48:49], s[0:1], exec
	s_waitcnt lgkmcnt(0)
	v_pk_mul_f32 v[16:17], v[16:17], v[126:127] op_sel_hi:[1,0]
	v_pk_mul_f32 v[14:15], v[14:15], v[126:127] op_sel_hi:[1,0]
	v_pk_mul_f32 v[12:13], v[12:13], v[126:127] op_sel_hi:[1,0]
	v_pk_mul_f32 v[10:11], v[10:11], v[126:127] op_sel_hi:[1,0]
	v_pk_mul_f32 v[8:9], v[8:9], v[126:127] op_sel_hi:[1,0]
	v_pk_mul_f32 v[6:7], v[6:7], v[126:127] op_sel_hi:[1,0]
	v_pk_mul_f32 v[4:5], v[4:5], v[126:127] op_sel_hi:[1,0]
	v_pk_mul_f32 v[2:3], v[2:3], v[126:127] op_sel_hi:[1,0]
	v_mfma_f32_32x32x16_bf16 v[82:97], v[122:125], v[114:117], v[82:97]
	ds_read_b128 v[78:81], v177 offset:33792
	ds_read_b128 v[122:125], v177 offset:34816
	v_mul_f32_e64 v32, v32, v126
	v_mul_f32_e64 v33, v33, v126
	v_mul_f32_e64 v30, v30, v126
	v_mul_f32_e64 v31, v31, v126
	v_pk_mul_f32 v[28:29], v[28:29], v[126:127] op_sel_hi:[1,0]
	v_pk_mul_f32 v[26:27], v[26:27], v[126:127] op_sel_hi:[1,0]
	v_pk_mul_f32 v[24:25], v[24:25], v[126:127] op_sel_hi:[1,0]
	v_pk_mul_f32 v[22:23], v[22:23], v[126:127] op_sel_hi:[1,0]
	v_mfma_f32_32x32x16_bf16 v[2:17], v[134:137], v[66:69], v[2:17]
	v_mul_f32_e64 v20, v20, v126
	v_mul_f32_e64 v21, v21, v126
	v_mul_f32_e64 v18, v18, v126
	v_mul_f32_e64 v19, v19, v126
	v_mul_f32_e64 v48, v48, v126
	v_mul_f32_e64 v49, v49, v126
	v_pk_mul_f32 v[46:47], v[46:47], v[126:127] op_sel_hi:[1,0]
	v_pk_mul_f32 v[44:45], v[44:45], v[126:127] op_sel_hi:[1,0]
	v_pk_mul_f32 v[42:43], v[42:43], v[126:127] op_sel_hi:[1,0]
	v_pk_mul_f32 v[40:41], v[40:41], v[126:127] op_sel_hi:[1,0]
	s_waitcnt lgkmcnt(0)
	v_mfma_f32_32x32x16_bf16 v[2:17], v[78:81], v[74:77], v[2:17]
	v_mul_f32_e64 v38, v38, v126
	v_mul_f32_e64 v39, v39, v126
	v_mul_f32_e64 v36, v36, v126
	v_mul_f32_e64 v37, v37, v126
	v_mul_f32_e64 v34, v34, v126
	v_mul_f32_e64 v35, v35, v126
	v_pk_mul_f32 v[64:65], v[64:65], v[126:127] op_sel_hi:[1,0]
	v_pk_mul_f32 v[62:63], v[62:63], v[126:127] op_sel_hi:[1,0]
	v_pk_mul_f32 v[60:61], v[60:61], v[126:127] op_sel_hi:[1,0]
	v_pk_mul_f32 v[58:59], v[58:59], v[126:127] op_sel_hi:[1,0]
	v_mfma_f32_32x32x16_bf16 v[2:17], v[122:125], v[114:117], v[2:17]
	ds_read_b128 v[78:81], v177 offset:35840
	ds_read_b128 v[122:125], v177 offset:36864
	v_mul_f32_e64 v56, v56, v126
	v_mul_f32_e64 v57, v57, v126
	v_mul_f32_e64 v54, v54, v126
	v_mul_f32_e64 v55, v55, v126
	v_pk_mul_f32 v[52:53], v[52:53], v[126:127] op_sel_hi:[1,0]
	v_pk_mul_f32 v[50:51], v[50:51], v[126:127] op_sel_hi:[1,0]
	s_cselect_b32 s64, s64, s65
	s_cmp_gt_i32 s64, 3
	s_waitcnt lgkmcnt(0)
	v_mfma_f32_32x32x16_bf16 v[18:33], v[122:125], v[66:69], v[18:33]
	s_cselect_b64 s[48:49], -1, 0
	s_cmp_lt_i32 s64, 4
	v_mfma_f32_32x32x16_bf16 v[2:17], v[78:81], v[118:121], v[2:17]
	ds_read_b128 v[78:81], v177 offset:37888
	ds_read_b128 v[122:125], v177 offset:38912
	s_waitcnt lgkmcnt(0)
	v_mfma_f32_32x32x16_bf16 v[18:33], v[78:81], v[74:77], v[18:33]
	v_mfma_f32_32x32x16_bf16 v[18:33], v[122:125], v[114:117], v[18:33]
	ds_read_b128 v[78:81], v177 offset:39936
	ds_read_b128 v[122:125], v177 offset:40960
	s_waitcnt lgkmcnt(0)
	v_mfma_f32_32x32x16_bf16 v[34:49], v[122:125], v[66:69], v[34:49]
	v_mfma_f32_32x32x16_bf16 v[18:33], v[78:81], v[118:121], v[18:33]
	ds_read_b128 v[78:81], v177 offset:41984
	ds_read_b128 v[122:125], v177 offset:43008
	s_waitcnt lgkmcnt(0)
	v_mfma_f32_32x32x16_bf16 v[34:49], v[78:81], v[74:77], v[34:49]
	v_mfma_f32_32x32x16_bf16 v[34:49], v[122:125], v[114:117], v[34:49]
	ds_read_b128 v[78:81], v177 offset:44032
	ds_read_b128 v[122:125], v177 offset:45056
	s_waitcnt lgkmcnt(0)
	v_mfma_f32_32x32x16_bf16 v[50:65], v[122:125], v[66:69], v[50:65]
	v_mfma_f32_32x32x16_bf16 v[34:49], v[78:81], v[118:121], v[34:49]
	ds_read_b128 v[66:69], v177 offset:46080
	ds_read_b128 v[78:81], v177 offset:47104
	s_waitcnt lgkmcnt(0)
	v_mfma_f32_32x32x16_bf16 v[50:65], v[66:69], v[74:77], v[50:65]
	v_mfma_f32_32x32x16_bf16 v[50:65], v[78:81], v[114:117], v[50:65]
	v_mfma_f32_32x32x16_bf16 v[82:97], v[130:133], v[118:121], v[82:97]
	v_mfma_f32_32x32x16_bf16 v[50:65], v[70:73], v[118:121], v[50:65]
	s_cbranch_scc1 .LBB0_630
; __device__ __forceinline__ bf16_t f2bf(float a) { return (bf16_t)(pk(a, 0.f) & 0xffffu); }
; __device__ __forceinline__ void p4_scan(Frame& F) {
;     ...
;         const int cidx = STEP_CIDX(n);
;         stored = cidx >= CTXL / 64;
;         if (cidx >= CTXL / 64) { const int rowbase = b * SEQ + (cidx - CTXL / 64) * 64;
; #pragma unroll
;             for (int mt = 0; mt < 2; ++mt)
; #pragma unroll
;                 for (int reg = 0; reg < 16; ++reg) { const int row = 32 * mt + (reg & 3) + 8 * (reg >> 2) + 4 * hh, prow = rowbase + (dir ? 63 - row : row);
;                     OGb[(size_t)prow * 1024 + h * 128 + 32 * nt + c] = f2bf(O[mt][reg]); } }
	s_lshl_b32 s64, s64, 6
	s_add_i32 s64, s61, s64
	v_or_b32_e32 v66, s64, v141
	v_cvt_pk_bf16_f32 v68, v98, s0
	v_lshl_add_u32 v66, v66, 11, v142
	global_store_short v66, v68, s[98:99]
	v_or_b32_e32 v66, s64, v144
	v_cvt_pk_bf16_f32 v68, v99, s0
	v_lshl_add_u32 v66, v66, 11, v142
	global_store_short v66, v68, s[98:99]
	v_or_b32_e32 v66, s64, v145
	v_cvt_pk_bf16_f32 v68, v100, s0
	v_lshl_add_u32 v66, v66, 11, v142
	global_store_short v66, v68, s[98:99]
	v_or_b32_e32 v66, s64, v146
	v_cvt_pk_bf16_f32 v68, v101, s0
	v_lshl_add_u32 v66, v66, 11, v142
	global_store_short v66, v68, s[98:99]
	v_or_b32_e32 v66, s64, v147
	v_cvt_pk_bf16_f32 v68, v102, s0
	v_lshl_add_u32 v66, v66, 11, v142
	global_store_short v66, v68, s[98:99]
	v_or_b32_e32 v66, s64, v148
	v_cvt_pk_bf16_f32 v68, v103, s0
	v_lshl_add_u32 v66, v66, 11, v142
	global_store_short v66, v68, s[98:99]
	v_or_b32_e32 v66, s64, v149
	v_cvt_pk_bf16_f32 v68, v104, s0
	v_lshl_add_u32 v66, v66, 11, v142
	global_store_short v66, v68, s[98:99]
	v_or_b32_e32 v66, s64, v150
	v_cvt_pk_bf16_f32 v68, v105, s0
	v_lshl_add_u32 v66, v66, 11, v142
	global_store_short v66, v68, s[98:99]
	v_or_b32_e32 v66, s64, v151
	v_cvt_pk_bf16_f32 v68, v106, s0
	v_lshl_add_u32 v66, v66, 11, v142
	global_store_short v66, v68, s[98:99]
	v_or_b32_e32 v66, s64, v152
	v_cvt_pk_bf16_f32 v68, v107, s0
	v_lshl_add_u32 v66, v66, 11, v142
	global_store_short v66, v68, s[98:99]
	v_or_b32_e32 v66, s64, v153
	v_cvt_pk_bf16_f32 v68, v108, s0
	v_lshl_add_u32 v66, v66, 11, v142
	global_store_short v66, v68, s[98:99]
	v_or_b32_e32 v66, s64, v154
	v_cvt_pk_bf16_f32 v68, v109, s0
	v_lshl_add_u32 v66, v66, 11, v142
	global_store_short v66, v68, s[98:99]
	v_or_b32_e32 v66, s64, v155
	v_cvt_pk_bf16_f32 v68, v110, s0
	v_lshl_add_u32 v66, v66, 11, v142
	global_store_short v66, v68, s[98:99]
	v_or_b32_e32 v66, s64, v156
	v_cvt_pk_bf16_f32 v68, v111, s0
	v_lshl_add_u32 v66, v66, 11, v142
	global_store_short v66, v68, s[98:99]
	v_or_b32_e32 v66, s64, v157
	v_cvt_pk_bf16_f32 v68, v112, s0
	v_lshl_add_u32 v66, v66, 11, v142
	global_store_short v66, v68, s[98:99]
	v_or_b32_e32 v66, s64, v158
	v_cvt_pk_bf16_f32 v68, v113, s0
	v_lshl_add_u32 v66, v66, 11, v142
	global_store_short v66, v68, s[98:99]
	v_or_b32_e32 v66, s64, v159
	v_cvt_pk_bf16_f32 v68, v82, s0
	v_lshl_add_u32 v66, v66, 11, v142
	global_store_short v66, v68, s[98:99]
	v_or_b32_e32 v66, s64, v160
	v_cvt_pk_bf16_f32 v68, v83, s0
	v_lshl_add_u32 v66, v66, 11, v142
	global_store_short v66, v68, s[98:99]
	v_or_b32_e32 v66, s64, v161
	v_cvt_pk_bf16_f32 v68, v84, s0
	v_lshl_add_u32 v66, v66, 11, v142
	global_store_short v66, v68, s[98:99]
	v_or_b32_e32 v66, s64, v163
	v_cvt_pk_bf16_f32 v68, v85, s0
	v_lshl_add_u32 v66, v66, 11, v142
	global_store_short v66, v68, s[98:99]
	v_or_b32_e32 v66, s64, v164
	v_cvt_pk_bf16_f32 v68, v86, s0
	v_lshl_add_u32 v66, v66, 11, v142
	global_store_short v66, v68, s[98:99]
	v_or_b32_e32 v66, s64, v165
	v_cvt_pk_bf16_f32 v68, v87, s0
	v_lshl_add_u32 v66, v66, 11, v142
	global_store_short v66, v68, s[98:99]
	v_or_b32_e32 v66, s64, v166
	v_cvt_pk_bf16_f32 v68, v88, s0
	v_lshl_add_u32 v66, v66, 11, v142
	global_store_short v66, v68, s[98:99]
	v_or_b32_e32 v66, s64, v167
	v_cvt_pk_bf16_f32 v68, v89, s0
	v_lshl_add_u32 v66, v66, 11, v142
	global_store_short v66, v68, s[98:99]
	v_or_b32_e32 v66, s64, v168
	v_cvt_pk_bf16_f32 v68, v90, s0
	v_lshl_add_u32 v66, v66, 11, v142
	global_store_short v66, v68, s[98:99]
	v_or_b32_e32 v66, s64, v169
	v_cvt_pk_bf16_f32 v68, v91, s0
	v_lshl_add_u32 v66, v66, 11, v142
	global_store_short v66, v68, s[98:99]
	v_or_b32_e32 v66, s64, v170
	v_cvt_pk_bf16_f32 v68, v92, s0
	v_lshl_add_u32 v66, v66, 11, v142
	global_store_short v66, v68, s[98:99]
	v_or_b32_e32 v66, s64, v171
	v_cvt_pk_bf16_f32 v68, v93, s0
	v_lshl_add_u32 v66, v66, 11, v142
	global_store_short v66, v68, s[98:99]
	v_or_b32_e32 v66, s64, v172
	v_cvt_pk_bf16_f32 v68, v94, s0
	v_lshl_add_u32 v66, v66, 11, v142
	global_store_short v66, v68, s[98:99]
	v_or_b32_e32 v66, s64, v173
	v_cvt_pk_bf16_f32 v68, v95, s0
	v_lshl_add_u32 v66, v66, 11, v142
	global_store_short v66, v68, s[98:99]
	v_or_b32_e32 v66, s64, v174
	v_cvt_pk_bf16_f32 v68, v96, s0
	v_lshl_add_u32 v66, v66, 11, v142
	global_store_short v66, v68, s[98:99]
	v_or_b32_e32 v66, s64, v175
	v_cvt_pk_bf16_f32 v68, v97, s0
	v_lshl_add_u32 v66, v66, 11, v142
	global_store_short v66, v68, s[98:99]
	s_branch .LBB0_630

; #define LAS __attribute__((address_space(3)))
; __global__ void __launch_bounds__(512, 2) fwd_kernel(Args args) {
;     extern __shared__ __attribute__((aligned(16))) unsigned char lds_raw[];
;     Frame F;
;     F.lds = (LAS unsigned char*)lds_raw; F.MISC = (volatile LAS unsigned*)(F.lds + MISC_OFF);
;     F.tid = threadIdx.x; F.lane = F.tid & 63; F.wave = __builtin_amdgcn_readfirstlane(F.tid >> 6); F.G = gridDim.x; F.bid = blockIdx.x;
	.amdhsa_kernel _Z10fwd_kernel4Args
		.amdhsa_group_segment_fixed_size 0
		.amdhsa_private_segment_fixed_size 0
		.amdhsa_kernarg_size 504
		.amdhsa_user_sgpr_count 2
		.amdhsa_user_sgpr_dispatch_ptr 0
		.amdhsa_user_sgpr_queue_ptr 0
		.amdhsa_user_sgpr_kernarg_segment_ptr 1
		.amdhsa_user_sgpr_dispatch_id 0
		.amdhsa_user_sgpr_kernarg_preload_length 0
		.amdhsa_user_sgpr_kernarg_preload_offset 0
		.amdhsa_user_sgpr_private_segment_size 0
		.amdhsa_uses_dynamic_stack 0
		.amdhsa_enable_private_segment 0
		.amdhsa_system_sgpr_workgroup_id_x 1
		.amdhsa_system_sgpr_workgroup_id_y 0
		.amdhsa_system_sgpr_workgroup_id_z 0
		.amdhsa_system_sgpr_workgroup_info 0
		.amdhsa_system_vgpr_workitem_id 0
		.amdhsa_next_free_vgpr 256
		.amdhsa_next_free_sgpr 102
		.amdhsa_accum_offset 256
		.amdhsa_reserve_vcc 1
		.amdhsa_float_round_mode_32 0
		.amdhsa_float_round_mode_16_64 0
		.amdhsa_float_denorm_mode_32 3
		.amdhsa_float_denorm_mode_16_64 3
		.amdhsa_dx10_clamp 1
		.amdhsa_ieee_mode 1
		.amdhsa_fp16_overflow 0
		.amdhsa_tg_split 0
		.amdhsa_exception_fp_ieee_invalid_op 0
		.amdhsa_exception_fp_denorm_src 0
		.amdhsa_exception_fp_ieee_div_zero 0
		.amdhsa_exception_fp_ieee_overflow 0
		.amdhsa_exception_fp_ieee_underflow 0
		.amdhsa_exception_fp_ieee_inexact 0
		.amdhsa_exception_int_div_zero 0
	.end_amdhsa_kernel

; #define LAS __attribute__((address_space(3)))
; __global__ void __launch_bounds__(512, 2) fwd_kernel(Args args) {
;     extern __shared__ __attribute__((aligned(16))) unsigned char lds_raw[];
;     Frame F;
;     F.lds = (LAS unsigned char*)lds_raw; F.MISC = (volatile LAS unsigned*)(F.lds + MISC_OFF);
;     F.tid = threadIdx.x; F.lane = F.tid & 63; F.wave = __builtin_amdgcn_readfirstlane(F.tid >> 6); F.G = gridDim.x; F.bid = blockIdx.x;
amdhsa.kernels:
  - .agpr_count:     0
    .args:
      - .offset:         0
        .size:           248
        .value_kind:     by_value
      - .offset:         248
        .size:           4
        .value_kind:     hidden_block_count_x
      - .offset:         252
        .size:           4
        .value_kind:     hidden_block_count_y
      - .offset:         256
        .size:           4
        .value_kind:     hidden_block_count_z
      - .offset:         260
        .size:           2
        .value_kind:     hidden_group_size_x
      - .offset:         262
        .size:           2
        .value_kind:     hidden_group_size_y
      - .offset:         264
        .size:           2
        .value_kind:     hidden_group_size_z
      - .offset:         266
        .size:           2
        .value_kind:     hidden_remainder_x
      - .offset:         268
        .size:           2
        .value_kind:     hidden_remainder_y
      - .offset:         270
        .size:           2
        .value_kind:     hidden_remainder_z
      - .offset:         288
        .size:           8
        .value_kind:     hidden_global_offset_x
      - .offset:         296
        .size:           8
        .value_kind:     hidden_global_offset_y
      - .offset:         304
        .size:           8
        .value_kind:     hidden_global_offset_z
      - .offset:         312
        .size:           2
        .value_kind:     hidden_grid_dims
      - .offset:         368
        .size:           4
        .value_kind:     hidden_dynamic_lds_size
    .group_segment_fixed_size: 0
    .kernarg_segment_align: 8
    .kernarg_segment_size: 504
    .language:       OpenCL C
    .language_version:
      - 2
      - 0
    .max_flat_workgroup_size: 512
    .name:           _Z10fwd_kernel4Args
    .private_segment_fixed_size: 0
    .sgpr_count:     108
    .sgpr_spill_count: 262
    .symbol:         _Z10fwd_kernel4Args.kd
    .uniform_work_group_size: 1
    .uses_dynamic_stack: false
    .vgpr_count:     256
    .vgpr_spill_count: 0
    .wavefront_size: 64
